# speedup vs baseline: 1.0179x; 1.0055x over previous
.Lkf_par_done:
	s_mov_b64 exec, -1
	v_lshlrev_b32_e32 v4, 16, v4
	v_lshlrev_b32_e32 v5, 24, v5
	v_lshl_or_b32 v3, v3, 8, v4
	v_lshlrev_b32_e32 v4, 16, v12
	v_or3_b32 v3, v3, v5, v2
	v_lshlrev_b32_e32 v5, 24, v13
	v_lshl_or_b32 v4, v11, 8, v4
	v_or3_b32 v43, v4, v5, v10
	v_lshlrev_b32_e32 v4, 16, v16
	v_lshlrev_b32_e32 v5, 24, v17
	v_lshl_or_b32 v4, v15, 8, v4
	v_lshlrev_b32_e32 v8, 16, v8
	v_or3_b32 v42, v4, v5, v14
	v_lshlrev_b32_e32 v4, 16, v20
	v_lshlrev_b32_e32 v9, 24, v9
	v_lshl_or_b32 v7, v7, 8, v8
	v_lshlrev_b32_e32 v5, 24, v21
	v_lshl_or_b32 v4, v19, 8, v4
	v_or3_b32 v44, v7, v9, v6
	v_or3_b32 v41, v4, v5, v18
	v_lshlrev_b32_e32 v4, 16, v24
	v_mov_b32_e32 v7, 0
	v_mov_b32_e32 v8, 0x64c
	v_lshlrev_b32_e32 v5, 24, v25
	v_lshl_or_b32 v4, v23, 8, v4
	s_waitcnt lgkmcnt(0)
	s_barrier
	ds_read_b96 v[36:38], v7 offset:1600
	ds_read_b64 v[16:17], v7 offset:1624
	ds_read2_b32 v[20:21], v8 offset1:1
	v_or3_b32 v19, v4, v5, v22
	v_lshlrev_b32_e32 v4, 16, v28
	v_lshlrev_b32_e32 v5, 24, v29
	v_lshl_or_b32 v4, v27, 8, v4
	v_or3_b32 v13, v4, v5, v26
	v_lshlrev_b32_e32 v4, 16, v32
	v_lshlrev_b32_e32 v5, 24, v33
	v_lshl_or_b32 v4, v31, 8, v4
	v_or3_b32 v9, v4, v5, v30
	ds_read_b32 v8, v7 offset:1620
	ds_read_b32 v12, v7 offset:1632
	ds_read_b128 v[30:33], v134 offset:49152
	s_movk_i32 s3, 0xfff
	v_mov_b32_e32 v11, 0x670
	v_mov_b32_e32 v15, 0x10000
	v_mov_b32_e32 v164, 1
	v_mov_b32_e32 v165, 2
	s_mov_b32 s16, 0xfff0fff0
	s_mov_b32 s17, 1
	s_mov_b32 s18, 2
	s_mov_b32 s19, 3
	s_waitcnt vmcnt(0) lgkmcnt(0)
	v_mov_b32_e32 v24, v38
	v_pk_fma_f32 v[22:23], v[76:77], v[20:21], v[16:17] op_sel_hi:[1,0,0]
	v_pk_fma_f32 v[22:23], v[78:79], v[36:37], v[22:23] op_sel_hi:[1,0,1]
	s_nop 0
	v_exp_f32_e32 v26, v22
	v_exp_f32_e32 v27, v23
	v_pk_fma_f32 v[154:155], v[76:77], v[20:21], v[16:17] op_sel:[0,1,1]
	v_cmp_eq_u32_sdwa vcc, s17, v44 src0_sel:DWORD src1_sel:BYTE_0
	v_pk_fma_f32 v[154:155], v[78:79], v[36:37], v[154:155] op_sel:[0,1,0]
	v_cvt_pknorm_u16_f32 v158, v26, v27
	v_and_b32_e32 v159, s16, v158
	v_exp_f32_e32 v156, v154
	v_cndmask_b32_e32 v162, v164, v15, vcc
	v_cndmask_b32_e32 v150, 0, v26, vcc
	v_exp_f32_e32 v157, v155
	v_cmp_eq_u32_sdwa vcc, s17, v44 src0_sel:DWORD src1_sel:BYTE_1
	v_lshrrev_b32_sdwa v160, v165, v159 dst_sel:DWORD dst_unused:UNUSED_PAD src0_sel:DWORD src1_sel:WORD_0
	v_lshrrev_b32_sdwa v161, v165, v159 dst_sel:DWORD dst_unused:UNUSED_PAD src0_sel:DWORD src1_sel:WORD_1
	v_cndmask_b32_e32 v163, v164, v15, vcc
	v_cndmask_b32_e32 v151, 0, v27, vcc
	v_pk_fma_f32 v[22:23], v[76:77], v[8:9], v[12:13] op_sel_hi:[1,0,0]
	v_cmp_eq_u32_sdwa vcc, s18, v44 src0_sel:DWORD src1_sel:BYTE_0
	v_pk_fma_f32 v[22:23], v[78:79], v[24:25], v[22:23] op_sel_hi:[1,0,1]
	ds_add_u32 v160, v162 offset:1648
	ds_add_u32 v161, v163 offset:1648
	v_cvt_pknorm_u16_f32 v158, v156, v157
	v_and_b32_e32 v159, s16, v158
	v_exp_f32_e32 v26, v22
	v_cndmask_b32_e32 v162, v164, v15, vcc
	v_cndmask_b32_e32 v150, v150, v156, vcc
	v_exp_f32_e32 v27, v23
	v_cmp_eq_u32_sdwa vcc, s18, v44 src0_sel:DWORD src1_sel:BYTE_1
	v_lshrrev_b32_sdwa v160, v165, v159 dst_sel:DWORD dst_unused:UNUSED_PAD src0_sel:DWORD src1_sel:WORD_0
	v_lshrrev_b32_sdwa v161, v165, v159 dst_sel:DWORD dst_unused:UNUSED_PAD src0_sel:DWORD src1_sel:WORD_1
	v_cndmask_b32_e32 v163, v164, v15, vcc
	v_cndmask_b32_e32 v151, v151, v157, vcc
	v_pk_fma_f32 v[154:155], v[80:81], v[20:21], v[16:17] op_sel_hi:[1,0,0]
	v_cmp_eq_u32_sdwa vcc, s19, v44 src0_sel:DWORD src1_sel:BYTE_0
	v_pk_fma_f32 v[154:155], v[82:83], v[36:37], v[154:155] op_sel_hi:[1,0,1]
	ds_add_u32 v160, v162 offset:18032
	ds_add_u32 v161, v163 offset:18032
	v_cvt_pknorm_u16_f32 v158, v26, v27
	v_and_b32_e32 v159, s16, v158
	v_exp_f32_e32 v156, v154
	v_cndmask_b32_e32 v162, v164, v15, vcc
	v_cndmask_b32_e32 v150, v150, v26, vcc
	v_exp_f32_e32 v157, v155
	v_cmp_eq_u32_sdwa vcc, s19, v44 src0_sel:DWORD src1_sel:BYTE_1
	v_lshrrev_b32_sdwa v160, v165, v159 dst_sel:DWORD dst_unused:UNUSED_PAD src0_sel:DWORD src1_sel:WORD_0
	v_lshrrev_b32_sdwa v161, v165, v159 dst_sel:DWORD dst_unused:UNUSED_PAD src0_sel:DWORD src1_sel:WORD_1
	v_cndmask_b32_e32 v163, v164, v15, vcc
	v_cndmask_b32_e32 v151, v151, v27, vcc
	s_waitcnt lgkmcnt(4)
	v_pk_add_f32 v[166:167], v[30:31], v[150:151] neg_lo:[0,1] neg_hi:[0,1]
	s_nop 0
	v_pk_mul_f32 v[166:167], v[166:167], v[166:167]
	v_pk_fma_f32 v[22:23], v[80:81], v[20:21], v[16:17] op_sel:[0,1,1]
	v_cmp_eq_u32_sdwa vcc, s17, v44 src0_sel:DWORD src1_sel:BYTE_2
	v_pk_fma_f32 v[22:23], v[82:83], v[36:37], v[22:23] op_sel:[0,1,0]
	ds_add_u32 v160, v162 offset:34416
	ds_add_u32 v161, v163 offset:34416
	v_cvt_pknorm_u16_f32 v158, v156, v157
	v_and_b32_e32 v159, s16, v158
	v_exp_f32_e32 v26, v22
	v_cndmask_b32_e32 v162, v164, v15, vcc
	v_cndmask_b32_e32 v152, 0, v156, vcc
	v_exp_f32_e32 v27, v23
	v_cmp_eq_u32_sdwa vcc, s17, v44 src0_sel:DWORD src1_sel:BYTE_3
	v_lshrrev_b32_sdwa v160, v165, v159 dst_sel:DWORD dst_unused:UNUSED_PAD src0_sel:DWORD src1_sel:WORD_0
	v_lshrrev_b32_sdwa v161, v165, v159 dst_sel:DWORD dst_unused:UNUSED_PAD src0_sel:DWORD src1_sel:WORD_1
	v_cndmask_b32_e32 v163, v164, v15, vcc
	v_cndmask_b32_e32 v153, 0, v157, vcc
	v_pk_fma_f32 v[154:155], v[80:81], v[8:9], v[12:13] op_sel_hi:[1,0,0]
	v_cmp_eq_u32_sdwa vcc, s18, v44 src0_sel:DWORD src1_sel:BYTE_2
	v_pk_fma_f32 v[154:155], v[82:83], v[24:25], v[154:155] op_sel_hi:[1,0,1]
	ds_add_u32 v160, v162 offset:1648
	ds_add_u32 v161, v163 offset:1648
	v_cvt_pknorm_u16_f32 v158, v26, v27
	v_and_b32_e32 v159, s16, v158
	v_exp_f32_e32 v156, v154
	v_cndmask_b32_e32 v162, v164, v15, vcc
	v_cndmask_b32_e32 v152, v152, v26, vcc
	v_exp_f32_e32 v157, v155
	v_cmp_eq_u32_sdwa vcc, s18, v44 src0_sel:DWORD src1_sel:BYTE_3
	v_lshrrev_b32_sdwa v160, v165, v159 dst_sel:DWORD dst_unused:UNUSED_PAD src0_sel:DWORD src1_sel:WORD_0
	v_lshrrev_b32_sdwa v161, v165, v159 dst_sel:DWORD dst_unused:UNUSED_PAD src0_sel:DWORD src1_sel:WORD_1
	v_cndmask_b32_e32 v163, v164, v15, vcc
	v_cndmask_b32_e32 v153, v153, v27, vcc
	v_cmp_eq_u32_sdwa vcc, s19, v44 src0_sel:DWORD src1_sel:BYTE_2
	ds_add_u32 v160, v162 offset:18032
	ds_add_u32 v161, v163 offset:18032
	v_cvt_pknorm_u16_f32 v158, v156, v157
	v_and_b32_e32 v159, s16, v158
	v_cndmask_b32_e32 v162, v164, v15, vcc
	v_cndmask_b32_e32 v152, v152, v156, vcc
	v_cmp_eq_u32_sdwa vcc, s19, v44 src0_sel:DWORD src1_sel:BYTE_3
	v_lshrrev_b32_sdwa v160, v165, v159 dst_sel:DWORD dst_unused:UNUSED_PAD src0_sel:DWORD src1_sel:WORD_0
	v_lshrrev_b32_sdwa v161, v165, v159 dst_sel:DWORD dst_unused:UNUSED_PAD src0_sel:DWORD src1_sel:WORD_1
	v_cndmask_b32_e32 v163, v164, v15, vcc
	v_cndmask_b32_e32 v153, v153, v157, vcc
	ds_add_u32 v160, v162 offset:34416
	ds_add_u32 v161, v163 offset:34416
	v_pk_add_f32 v[22:23], v[32:33], v[152:153] neg_lo:[0,1] neg_hi:[0,1]
	s_nop 0
	v_pk_fma_f32 v[28:29], v[22:23], v[22:23], v[166:167]
	ds_read_b128 v[76:79], v134 offset:61440
	v_pk_fma_f32 v[80:81], v[84:85], v[20:21], v[16:17] op_sel_hi:[1,0,0]
	v_pk_fma_f32 v[80:81], v[86:87], v[36:37], v[80:81] op_sel_hi:[1,0,1]
	s_nop 0
	v_exp_f32_e32 v82, v80
	v_exp_f32_e32 v83, v81
	v_pk_fma_f32 v[154:155], v[84:85], v[20:21], v[16:17] op_sel:[0,1,1]
	v_cmp_eq_u32_sdwa vcc, s17, v3 src0_sel:DWORD src1_sel:BYTE_0
	v_pk_fma_f32 v[154:155], v[86:87], v[36:37], v[154:155] op_sel:[0,1,0]
	v_cvt_pknorm_u16_f32 v158, v82, v83
	v_and_b32_e32 v159, s16, v158
	v_exp_f32_e32 v156, v154
	v_cndmask_b32_e32 v162, v164, v15, vcc
	v_cndmask_b32_e32 v150, 0, v82, vcc
	v_exp_f32_e32 v157, v155
	v_cmp_eq_u32_sdwa vcc, s17, v3 src0_sel:DWORD src1_sel:BYTE_1
	v_lshrrev_b32_sdwa v160, v165, v159 dst_sel:DWORD dst_unused:UNUSED_PAD src0_sel:DWORD src1_sel:WORD_0
	v_lshrrev_b32_sdwa v161, v165, v159 dst_sel:DWORD dst_unused:UNUSED_PAD src0_sel:DWORD src1_sel:WORD_1
	v_cndmask_b32_e32 v163, v164, v15, vcc
	v_cndmask_b32_e32 v151, 0, v83, vcc
	v_pk_fma_f32 v[80:81], v[84:85], v[8:9], v[12:13] op_sel_hi:[1,0,0]
	v_cmp_eq_u32_sdwa vcc, s18, v3 src0_sel:DWORD src1_sel:BYTE_0
	v_pk_fma_f32 v[80:81], v[86:87], v[24:25], v[80:81] op_sel_hi:[1,0,1]
	ds_add_u32 v160, v162 offset:1648
	ds_add_u32 v161, v163 offset:1648
	v_cvt_pknorm_u16_f32 v158, v156, v157
	v_and_b32_e32 v159, s16, v158
	v_exp_f32_e32 v82, v80
	v_cndmask_b32_e32 v162, v164, v15, vcc
	v_cndmask_b32_e32 v150, v150, v156, vcc
	v_exp_f32_e32 v83, v81
	v_cmp_eq_u32_sdwa vcc, s18, v3 src0_sel:DWORD src1_sel:BYTE_1
	v_lshrrev_b32_sdwa v160, v165, v159 dst_sel:DWORD dst_unused:UNUSED_PAD src0_sel:DWORD src1_sel:WORD_0
	v_lshrrev_b32_sdwa v161, v165, v159 dst_sel:DWORD dst_unused:UNUSED_PAD src0_sel:DWORD src1_sel:WORD_1
	v_cndmask_b32_e32 v163, v164, v15, vcc
	v_cndmask_b32_e32 v151, v151, v157, vcc
	v_pk_fma_f32 v[154:155], v[88:89], v[20:21], v[16:17] op_sel_hi:[1,0,0]
	v_cmp_eq_u32_sdwa vcc, s19, v3 src0_sel:DWORD src1_sel:BYTE_0
	v_pk_fma_f32 v[154:155], v[90:91], v[36:37], v[154:155] op_sel_hi:[1,0,1]
	ds_add_u32 v160, v162 offset:18032
	ds_add_u32 v161, v163 offset:18032
	v_cvt_pknorm_u16_f32 v158, v82, v83
	v_and_b32_e32 v159, s16, v158
	v_exp_f32_e32 v156, v154
	v_cndmask_b32_e32 v162, v164, v15, vcc
	v_cndmask_b32_e32 v150, v150, v82, vcc
	v_exp_f32_e32 v157, v155
	v_cmp_eq_u32_sdwa vcc, s19, v3 src0_sel:DWORD src1_sel:BYTE_1
	v_lshrrev_b32_sdwa v160, v165, v159 dst_sel:DWORD dst_unused:UNUSED_PAD src0_sel:DWORD src1_sel:WORD_0
	v_lshrrev_b32_sdwa v161, v165, v159 dst_sel:DWORD dst_unused:UNUSED_PAD src0_sel:DWORD src1_sel:WORD_1
	v_cndmask_b32_e32 v163, v164, v15, vcc
	v_cndmask_b32_e32 v151, v151, v83, vcc
	s_waitcnt lgkmcnt(4)
	v_pk_add_f32 v[166:167], v[76:77], v[150:151] neg_lo:[0,1] neg_hi:[0,1]
	s_nop 0
	v_pk_fma_f32 v[166:167], v[166:167], v[166:167], v[28:29]
	v_pk_fma_f32 v[80:81], v[88:89], v[20:21], v[16:17] op_sel:[0,1,1]
	v_cmp_eq_u32_sdwa vcc, s17, v3 src0_sel:DWORD src1_sel:BYTE_2
	v_pk_fma_f32 v[80:81], v[90:91], v[36:37], v[80:81] op_sel:[0,1,0]
	ds_add_u32 v160, v162 offset:34416
	ds_add_u32 v161, v163 offset:34416
	v_cvt_pknorm_u16_f32 v158, v156, v157
	v_and_b32_e32 v159, s16, v158
	v_exp_f32_e32 v82, v80
	v_cndmask_b32_e32 v162, v164, v15, vcc
	v_cndmask_b32_e32 v152, 0, v156, vcc
	v_exp_f32_e32 v83, v81
	v_cmp_eq_u32_sdwa vcc, s17, v3 src0_sel:DWORD src1_sel:BYTE_3
	v_lshrrev_b32_sdwa v160, v165, v159 dst_sel:DWORD dst_unused:UNUSED_PAD src0_sel:DWORD src1_sel:WORD_0
	v_lshrrev_b32_sdwa v161, v165, v159 dst_sel:DWORD dst_unused:UNUSED_PAD src0_sel:DWORD src1_sel:WORD_1
	v_cndmask_b32_e32 v163, v164, v15, vcc
	v_cndmask_b32_e32 v153, 0, v157, vcc
	v_pk_fma_f32 v[154:155], v[88:89], v[8:9], v[12:13] op_sel_hi:[1,0,0]
	v_cmp_eq_u32_sdwa vcc, s18, v3 src0_sel:DWORD src1_sel:BYTE_2
	v_pk_fma_f32 v[154:155], v[90:91], v[24:25], v[154:155] op_sel_hi:[1,0,1]
	ds_add_u32 v160, v162 offset:1648
	ds_add_u32 v161, v163 offset:1648
	v_cvt_pknorm_u16_f32 v158, v82, v83
	v_and_b32_e32 v159, s16, v158
	v_exp_f32_e32 v156, v154
	v_cndmask_b32_e32 v162, v164, v15, vcc
	v_cndmask_b32_e32 v152, v152, v82, vcc
	v_exp_f32_e32 v157, v155
	v_cmp_eq_u32_sdwa vcc, s18, v3 src0_sel:DWORD src1_sel:BYTE_3
	v_lshrrev_b32_sdwa v160, v165, v159 dst_sel:DWORD dst_unused:UNUSED_PAD src0_sel:DWORD src1_sel:WORD_0
	v_lshrrev_b32_sdwa v161, v165, v159 dst_sel:DWORD dst_unused:UNUSED_PAD src0_sel:DWORD src1_sel:WORD_1
	v_cndmask_b32_e32 v163, v164, v15, vcc
	v_cndmask_b32_e32 v153, v153, v83, vcc
	v_cmp_eq_u32_sdwa vcc, s19, v3 src0_sel:DWORD src1_sel:BYTE_2
	ds_add_u32 v160, v162 offset:18032
	ds_add_u32 v161, v163 offset:18032
	v_cvt_pknorm_u16_f32 v158, v156, v157
	v_and_b32_e32 v159, s16, v158
	v_cndmask_b32_e32 v162, v164, v15, vcc
	v_cndmask_b32_e32 v152, v152, v156, vcc
	v_cmp_eq_u32_sdwa vcc, s19, v3 src0_sel:DWORD src1_sel:BYTE_3
	v_lshrrev_b32_sdwa v160, v165, v159 dst_sel:DWORD dst_unused:UNUSED_PAD src0_sel:DWORD src1_sel:WORD_0
	v_lshrrev_b32_sdwa v161, v165, v159 dst_sel:DWORD dst_unused:UNUSED_PAD src0_sel:DWORD src1_sel:WORD_1
	v_cndmask_b32_e32 v163, v164, v15, vcc
	v_cndmask_b32_e32 v153, v153, v157, vcc
	ds_add_u32 v160, v162 offset:34416
	ds_add_u32 v161, v163 offset:34416
	v_pk_add_f32 v[80:81], v[78:79], v[152:153] neg_lo:[0,1] neg_hi:[0,1]
	s_nop 0
	v_pk_fma_f32 v[6:7], v[80:81], v[80:81], v[166:167]
	ds_read_b128 v[76:79], v1 offset:24576
	v_pk_fma_f32 v[80:81], v[92:93], v[20:21], v[16:17] op_sel_hi:[1,0,0]
	v_pk_fma_f32 v[80:81], v[94:95], v[36:37], v[80:81] op_sel_hi:[1,0,1]
	s_nop 0
	v_exp_f32_e32 v82, v80
	v_exp_f32_e32 v83, v81
	v_pk_fma_f32 v[154:155], v[92:93], v[20:21], v[16:17] op_sel:[0,1,1]
	v_cmp_eq_u32_sdwa vcc, s17, v43 src0_sel:DWORD src1_sel:BYTE_0
	v_pk_fma_f32 v[154:155], v[94:95], v[36:37], v[154:155] op_sel:[0,1,0]
	v_cvt_pknorm_u16_f32 v158, v82, v83
	v_and_b32_e32 v159, s16, v158
	v_exp_f32_e32 v156, v154
	v_cndmask_b32_e32 v162, v164, v15, vcc
	v_cndmask_b32_e32 v150, 0, v82, vcc
	v_exp_f32_e32 v157, v155
	v_cmp_eq_u32_sdwa vcc, s17, v43 src0_sel:DWORD src1_sel:BYTE_1
	v_lshrrev_b32_sdwa v160, v165, v159 dst_sel:DWORD dst_unused:UNUSED_PAD src0_sel:DWORD src1_sel:WORD_0
	v_lshrrev_b32_sdwa v161, v165, v159 dst_sel:DWORD dst_unused:UNUSED_PAD src0_sel:DWORD src1_sel:WORD_1
	v_cndmask_b32_e32 v163, v164, v15, vcc
	v_cndmask_b32_e32 v151, 0, v83, vcc
	v_pk_fma_f32 v[80:81], v[92:93], v[8:9], v[12:13] op_sel_hi:[1,0,0]
	v_cmp_eq_u32_sdwa vcc, s18, v43 src0_sel:DWORD src1_sel:BYTE_0
	v_pk_fma_f32 v[80:81], v[94:95], v[24:25], v[80:81] op_sel_hi:[1,0,1]
	ds_add_u32 v160, v162 offset:1648
	ds_add_u32 v161, v163 offset:1648
	v_cvt_pknorm_u16_f32 v158, v156, v157
	v_and_b32_e32 v159, s16, v158
	v_exp_f32_e32 v82, v80
	v_cndmask_b32_e32 v162, v164, v15, vcc
	v_cndmask_b32_e32 v150, v150, v156, vcc
	v_exp_f32_e32 v83, v81
	v_cmp_eq_u32_sdwa vcc, s18, v43 src0_sel:DWORD src1_sel:BYTE_1
	v_lshrrev_b32_sdwa v160, v165, v159 dst_sel:DWORD dst_unused:UNUSED_PAD src0_sel:DWORD src1_sel:WORD_0
	v_lshrrev_b32_sdwa v161, v165, v159 dst_sel:DWORD dst_unused:UNUSED_PAD src0_sel:DWORD src1_sel:WORD_1
	v_cndmask_b32_e32 v163, v164, v15, vcc
	v_cndmask_b32_e32 v151, v151, v157, vcc
	v_pk_fma_f32 v[154:155], v[96:97], v[20:21], v[16:17] op_sel_hi:[1,0,0]
	v_cmp_eq_u32_sdwa vcc, s19, v43 src0_sel:DWORD src1_sel:BYTE_0
	v_pk_fma_f32 v[154:155], v[98:99], v[36:37], v[154:155] op_sel_hi:[1,0,1]
	ds_add_u32 v160, v162 offset:18032
	ds_add_u32 v161, v163 offset:18032
	v_cvt_pknorm_u16_f32 v158, v82, v83
	v_and_b32_e32 v159, s16, v158
	v_exp_f32_e32 v156, v154
	v_cndmask_b32_e32 v162, v164, v15, vcc
	v_cndmask_b32_e32 v150, v150, v82, vcc
	v_exp_f32_e32 v157, v155
	v_cmp_eq_u32_sdwa vcc, s19, v43 src0_sel:DWORD src1_sel:BYTE_1
	v_lshrrev_b32_sdwa v160, v165, v159 dst_sel:DWORD dst_unused:UNUSED_PAD src0_sel:DWORD src1_sel:WORD_0
	v_lshrrev_b32_sdwa v161, v165, v159 dst_sel:DWORD dst_unused:UNUSED_PAD src0_sel:DWORD src1_sel:WORD_1
	v_cndmask_b32_e32 v163, v164, v15, vcc
	v_cndmask_b32_e32 v151, v151, v83, vcc
	s_waitcnt lgkmcnt(4)
	v_pk_add_f32 v[166:167], v[76:77], v[150:151] neg_lo:[0,1] neg_hi:[0,1]
	s_nop 0
	v_pk_fma_f32 v[166:167], v[166:167], v[166:167], v[6:7]
	v_pk_fma_f32 v[80:81], v[96:97], v[20:21], v[16:17] op_sel:[0,1,1]
	v_cmp_eq_u32_sdwa vcc, s17, v43 src0_sel:DWORD src1_sel:BYTE_2
	v_pk_fma_f32 v[80:81], v[98:99], v[36:37], v[80:81] op_sel:[0,1,0]
	ds_add_u32 v160, v162 offset:34416
	ds_add_u32 v161, v163 offset:34416
	v_cvt_pknorm_u16_f32 v158, v156, v157
	v_and_b32_e32 v159, s16, v158
	v_exp_f32_e32 v82, v80
	v_cndmask_b32_e32 v162, v164, v15, vcc
	v_cndmask_b32_e32 v152, 0, v156, vcc
	v_exp_f32_e32 v83, v81
	v_cmp_eq_u32_sdwa vcc, s17, v43 src0_sel:DWORD src1_sel:BYTE_3
	v_lshrrev_b32_sdwa v160, v165, v159 dst_sel:DWORD dst_unused:UNUSED_PAD src0_sel:DWORD src1_sel:WORD_0
	v_lshrrev_b32_sdwa v161, v165, v159 dst_sel:DWORD dst_unused:UNUSED_PAD src0_sel:DWORD src1_sel:WORD_1
	v_cndmask_b32_e32 v163, v164, v15, vcc
	v_cndmask_b32_e32 v153, 0, v157, vcc
	v_pk_fma_f32 v[154:155], v[96:97], v[8:9], v[12:13] op_sel_hi:[1,0,0]
	v_cmp_eq_u32_sdwa vcc, s18, v43 src0_sel:DWORD src1_sel:BYTE_2
	v_pk_fma_f32 v[154:155], v[98:99], v[24:25], v[154:155] op_sel_hi:[1,0,1]
	ds_add_u32 v160, v162 offset:1648
	ds_add_u32 v161, v163 offset:1648
	v_cvt_pknorm_u16_f32 v158, v82, v83
	v_and_b32_e32 v159, s16, v158
	v_exp_f32_e32 v156, v154
	v_cndmask_b32_e32 v162, v164, v15, vcc
	v_cndmask_b32_e32 v152, v152, v82, vcc
	v_exp_f32_e32 v157, v155
	v_cmp_eq_u32_sdwa vcc, s18, v43 src0_sel:DWORD src1_sel:BYTE_3
	v_lshrrev_b32_sdwa v160, v165, v159 dst_sel:DWORD dst_unused:UNUSED_PAD src0_sel:DWORD src1_sel:WORD_0
	v_lshrrev_b32_sdwa v161, v165, v159 dst_sel:DWORD dst_unused:UNUSED_PAD src0_sel:DWORD src1_sel:WORD_1
	v_cndmask_b32_e32 v163, v164, v15, vcc
	v_cndmask_b32_e32 v153, v153, v83, vcc
	v_cmp_eq_u32_sdwa vcc, s19, v43 src0_sel:DWORD src1_sel:BYTE_2
	ds_add_u32 v160, v162 offset:18032
	ds_add_u32 v161, v163 offset:18032
	v_cvt_pknorm_u16_f32 v158, v156, v157
	v_and_b32_e32 v159, s16, v158
	v_cndmask_b32_e32 v162, v164, v15, vcc
	v_cndmask_b32_e32 v152, v152, v156, vcc
	v_cmp_eq_u32_sdwa vcc, s19, v43 src0_sel:DWORD src1_sel:BYTE_3
	v_lshrrev_b32_sdwa v160, v165, v159 dst_sel:DWORD dst_unused:UNUSED_PAD src0_sel:DWORD src1_sel:WORD_0
	v_lshrrev_b32_sdwa v161, v165, v159 dst_sel:DWORD dst_unused:UNUSED_PAD src0_sel:DWORD src1_sel:WORD_1
	v_cndmask_b32_e32 v163, v164, v15, vcc
	v_cndmask_b32_e32 v153, v153, v157, vcc
	ds_add_u32 v160, v162 offset:34416
	ds_add_u32 v161, v163 offset:34416
	v_pk_add_f32 v[80:81], v[78:79], v[152:153] neg_lo:[0,1] neg_hi:[0,1]
	s_nop 0
	v_pk_fma_f32 v[6:7], v[80:81], v[80:81], v[166:167]
	ds_read_b128 v[76:79], v1 offset:36864
	v_pk_fma_f32 v[80:81], v[100:101], v[20:21], v[16:17] op_sel_hi:[1,0,0]
	v_pk_fma_f32 v[80:81], v[102:103], v[36:37], v[80:81] op_sel_hi:[1,0,1]
	s_nop 0
	v_exp_f32_e32 v82, v80
	v_exp_f32_e32 v83, v81
	v_pk_fma_f32 v[154:155], v[100:101], v[20:21], v[16:17] op_sel:[0,1,1]
	v_cmp_eq_u32_sdwa vcc, s17, v42 src0_sel:DWORD src1_sel:BYTE_0
	v_pk_fma_f32 v[154:155], v[102:103], v[36:37], v[154:155] op_sel:[0,1,0]
	v_cvt_pknorm_u16_f32 v158, v82, v83
	v_and_b32_e32 v159, s16, v158
	v_exp_f32_e32 v156, v154
	v_cndmask_b32_e32 v162, v164, v15, vcc
	v_cndmask_b32_e32 v150, 0, v82, vcc
	v_exp_f32_e32 v157, v155
	v_cmp_eq_u32_sdwa vcc, s17, v42 src0_sel:DWORD src1_sel:BYTE_1
	v_lshrrev_b32_sdwa v160, v165, v159 dst_sel:DWORD dst_unused:UNUSED_PAD src0_sel:DWORD src1_sel:WORD_0
	v_lshrrev_b32_sdwa v161, v165, v159 dst_sel:DWORD dst_unused:UNUSED_PAD src0_sel:DWORD src1_sel:WORD_1
	v_cndmask_b32_e32 v163, v164, v15, vcc
	v_cndmask_b32_e32 v151, 0, v83, vcc
	v_pk_fma_f32 v[80:81], v[100:101], v[8:9], v[12:13] op_sel_hi:[1,0,0]
	v_cmp_eq_u32_sdwa vcc, s18, v42 src0_sel:DWORD src1_sel:BYTE_0
	v_pk_fma_f32 v[80:81], v[102:103], v[24:25], v[80:81] op_sel_hi:[1,0,1]
	ds_add_u32 v160, v162 offset:1648
	ds_add_u32 v161, v163 offset:1648
	v_cvt_pknorm_u16_f32 v158, v156, v157
	v_and_b32_e32 v159, s16, v158
	v_exp_f32_e32 v82, v80
	v_cndmask_b32_e32 v162, v164, v15, vcc
	v_cndmask_b32_e32 v150, v150, v156, vcc
	v_exp_f32_e32 v83, v81
	v_cmp_eq_u32_sdwa vcc, s18, v42 src0_sel:DWORD src1_sel:BYTE_1
	v_lshrrev_b32_sdwa v160, v165, v159 dst_sel:DWORD dst_unused:UNUSED_PAD src0_sel:DWORD src1_sel:WORD_0
	v_lshrrev_b32_sdwa v161, v165, v159 dst_sel:DWORD dst_unused:UNUSED_PAD src0_sel:DWORD src1_sel:WORD_1
	v_cndmask_b32_e32 v163, v164, v15, vcc
	v_cndmask_b32_e32 v151, v151, v157, vcc
	v_pk_fma_f32 v[154:155], v[104:105], v[20:21], v[16:17] op_sel_hi:[1,0,0]
	v_cmp_eq_u32_sdwa vcc, s19, v42 src0_sel:DWORD src1_sel:BYTE_0
	v_pk_fma_f32 v[154:155], v[106:107], v[36:37], v[154:155] op_sel_hi:[1,0,1]
	ds_add_u32 v160, v162 offset:18032
	ds_add_u32 v161, v163 offset:18032
	v_cvt_pknorm_u16_f32 v158, v82, v83
	v_and_b32_e32 v159, s16, v158
	v_exp_f32_e32 v156, v154
	v_cndmask_b32_e32 v162, v164, v15, vcc
	v_cndmask_b32_e32 v150, v150, v82, vcc
	v_exp_f32_e32 v157, v155
	v_cmp_eq_u32_sdwa vcc, s19, v42 src0_sel:DWORD src1_sel:BYTE_1
	v_lshrrev_b32_sdwa v160, v165, v159 dst_sel:DWORD dst_unused:UNUSED_PAD src0_sel:DWORD src1_sel:WORD_0
	v_lshrrev_b32_sdwa v161, v165, v159 dst_sel:DWORD dst_unused:UNUSED_PAD src0_sel:DWORD src1_sel:WORD_1
	v_cndmask_b32_e32 v163, v164, v15, vcc
	v_cndmask_b32_e32 v151, v151, v83, vcc
	s_waitcnt lgkmcnt(4)
	v_pk_add_f32 v[166:167], v[76:77], v[150:151] neg_lo:[0,1] neg_hi:[0,1]
	s_nop 0
	v_pk_fma_f32 v[166:167], v[166:167], v[166:167], v[6:7]
	v_pk_fma_f32 v[80:81], v[104:105], v[20:21], v[16:17] op_sel:[0,1,1]
	v_cmp_eq_u32_sdwa vcc, s17, v42 src0_sel:DWORD src1_sel:BYTE_2
	v_pk_fma_f32 v[80:81], v[106:107], v[36:37], v[80:81] op_sel:[0,1,0]
	ds_add_u32 v160, v162 offset:34416
	ds_add_u32 v161, v163 offset:34416
	v_cvt_pknorm_u16_f32 v158, v156, v157
	v_and_b32_e32 v159, s16, v158
	v_exp_f32_e32 v82, v80
	v_cndmask_b32_e32 v162, v164, v15, vcc
	v_cndmask_b32_e32 v152, 0, v156, vcc
	v_exp_f32_e32 v83, v81
	v_cmp_eq_u32_sdwa vcc, s17, v42 src0_sel:DWORD src1_sel:BYTE_3
	v_lshrrev_b32_sdwa v160, v165, v159 dst_sel:DWORD dst_unused:UNUSED_PAD src0_sel:DWORD src1_sel:WORD_0
	v_lshrrev_b32_sdwa v161, v165, v159 dst_sel:DWORD dst_unused:UNUSED_PAD src0_sel:DWORD src1_sel:WORD_1
	v_cndmask_b32_e32 v163, v164, v15, vcc
	v_cndmask_b32_e32 v153, 0, v157, vcc
	v_pk_fma_f32 v[154:155], v[104:105], v[8:9], v[12:13] op_sel_hi:[1,0,0]
	v_cmp_eq_u32_sdwa vcc, s18, v42 src0_sel:DWORD src1_sel:BYTE_2
	v_pk_fma_f32 v[154:155], v[106:107], v[24:25], v[154:155] op_sel_hi:[1,0,1]
	ds_add_u32 v160, v162 offset:1648
	ds_add_u32 v161, v163 offset:1648
	v_cvt_pknorm_u16_f32 v158, v82, v83
	v_and_b32_e32 v159, s16, v158
	v_exp_f32_e32 v156, v154
	v_cndmask_b32_e32 v162, v164, v15, vcc
	v_cndmask_b32_e32 v152, v152, v82, vcc
	v_exp_f32_e32 v157, v155
	v_cmp_eq_u32_sdwa vcc, s18, v42 src0_sel:DWORD src1_sel:BYTE_3
	v_lshrrev_b32_sdwa v160, v165, v159 dst_sel:DWORD dst_unused:UNUSED_PAD src0_sel:DWORD src1_sel:WORD_0
	v_lshrrev_b32_sdwa v161, v165, v159 dst_sel:DWORD dst_unused:UNUSED_PAD src0_sel:DWORD src1_sel:WORD_1
	v_cndmask_b32_e32 v163, v164, v15, vcc
	v_cndmask_b32_e32 v153, v153, v83, vcc
	v_cmp_eq_u32_sdwa vcc, s19, v42 src0_sel:DWORD src1_sel:BYTE_2
	ds_add_u32 v160, v162 offset:18032
	ds_add_u32 v161, v163 offset:18032
	v_cvt_pknorm_u16_f32 v158, v156, v157
	v_and_b32_e32 v159, s16, v158
	v_cndmask_b32_e32 v162, v164, v15, vcc
	v_cndmask_b32_e32 v152, v152, v156, vcc
	v_cmp_eq_u32_sdwa vcc, s19, v42 src0_sel:DWORD src1_sel:BYTE_3
	v_lshrrev_b32_sdwa v160, v165, v159 dst_sel:DWORD dst_unused:UNUSED_PAD src0_sel:DWORD src1_sel:WORD_0
	v_lshrrev_b32_sdwa v161, v165, v159 dst_sel:DWORD dst_unused:UNUSED_PAD src0_sel:DWORD src1_sel:WORD_1
	v_cndmask_b32_e32 v163, v164, v15, vcc
	v_cndmask_b32_e32 v153, v153, v157, vcc
	ds_add_u32 v160, v162 offset:34416
	ds_add_u32 v161, v163 offset:34416
	v_pk_add_f32 v[80:81], v[78:79], v[152:153] neg_lo:[0,1] neg_hi:[0,1]
	s_nop 0
	v_pk_fma_f32 v[6:7], v[80:81], v[80:81], v[166:167]
	ds_read_b128 v[76:79], v1 offset:49152
	v_pk_fma_f32 v[80:81], v[108:109], v[20:21], v[16:17] op_sel_hi:[1,0,0]
	v_pk_fma_f32 v[80:81], v[110:111], v[36:37], v[80:81] op_sel_hi:[1,0,1]
	s_nop 0
	v_exp_f32_e32 v82, v80
	v_exp_f32_e32 v83, v81
	v_pk_fma_f32 v[154:155], v[108:109], v[20:21], v[16:17] op_sel:[0,1,1]
	v_cmp_eq_u32_sdwa vcc, s17, v41 src0_sel:DWORD src1_sel:BYTE_0
	v_pk_fma_f32 v[154:155], v[110:111], v[36:37], v[154:155] op_sel:[0,1,0]
	v_cvt_pknorm_u16_f32 v158, v82, v83
	v_and_b32_e32 v159, s16, v158
	v_exp_f32_e32 v156, v154
	v_cndmask_b32_e32 v162, v164, v15, vcc
	v_cndmask_b32_e32 v150, 0, v82, vcc
	v_exp_f32_e32 v157, v155
	v_cmp_eq_u32_sdwa vcc, s17, v41 src0_sel:DWORD src1_sel:BYTE_1
	v_lshrrev_b32_sdwa v160, v165, v159 dst_sel:DWORD dst_unused:UNUSED_PAD src0_sel:DWORD src1_sel:WORD_0
	v_lshrrev_b32_sdwa v161, v165, v159 dst_sel:DWORD dst_unused:UNUSED_PAD src0_sel:DWORD src1_sel:WORD_1
	v_cndmask_b32_e32 v163, v164, v15, vcc
	v_cndmask_b32_e32 v151, 0, v83, vcc
	v_pk_fma_f32 v[80:81], v[108:109], v[8:9], v[12:13] op_sel_hi:[1,0,0]
	v_cmp_eq_u32_sdwa vcc, s18, v41 src0_sel:DWORD src1_sel:BYTE_0
	v_pk_fma_f32 v[80:81], v[110:111], v[24:25], v[80:81] op_sel_hi:[1,0,1]
	ds_add_u32 v160, v162 offset:1648
	ds_add_u32 v161, v163 offset:1648
	v_cvt_pknorm_u16_f32 v158, v156, v157
	v_and_b32_e32 v159, s16, v158
	v_exp_f32_e32 v82, v80
	v_cndmask_b32_e32 v162, v164, v15, vcc
	v_cndmask_b32_e32 v150, v150, v156, vcc
	v_exp_f32_e32 v83, v81
	v_cmp_eq_u32_sdwa vcc, s18, v41 src0_sel:DWORD src1_sel:BYTE_1
	v_lshrrev_b32_sdwa v160, v165, v159 dst_sel:DWORD dst_unused:UNUSED_PAD src0_sel:DWORD src1_sel:WORD_0
	v_lshrrev_b32_sdwa v161, v165, v159 dst_sel:DWORD dst_unused:UNUSED_PAD src0_sel:DWORD src1_sel:WORD_1
	v_cndmask_b32_e32 v163, v164, v15, vcc
	v_cndmask_b32_e32 v151, v151, v157, vcc
	v_pk_fma_f32 v[154:155], v[112:113], v[20:21], v[16:17] op_sel_hi:[1,0,0]
	v_cmp_eq_u32_sdwa vcc, s19, v41 src0_sel:DWORD src1_sel:BYTE_0
	v_pk_fma_f32 v[154:155], v[114:115], v[36:37], v[154:155] op_sel_hi:[1,0,1]
	ds_add_u32 v160, v162 offset:18032
	ds_add_u32 v161, v163 offset:18032
	v_cvt_pknorm_u16_f32 v158, v82, v83
	v_and_b32_e32 v159, s16, v158
	v_exp_f32_e32 v156, v154
	v_cndmask_b32_e32 v162, v164, v15, vcc
	v_cndmask_b32_e32 v150, v150, v82, vcc
	v_exp_f32_e32 v157, v155
	v_cmp_eq_u32_sdwa vcc, s19, v41 src0_sel:DWORD src1_sel:BYTE_1
	v_lshrrev_b32_sdwa v160, v165, v159 dst_sel:DWORD dst_unused:UNUSED_PAD src0_sel:DWORD src1_sel:WORD_0
	v_lshrrev_b32_sdwa v161, v165, v159 dst_sel:DWORD dst_unused:UNUSED_PAD src0_sel:DWORD src1_sel:WORD_1
	v_cndmask_b32_e32 v163, v164, v15, vcc
	v_cndmask_b32_e32 v151, v151, v83, vcc
	s_waitcnt lgkmcnt(4)
	v_pk_add_f32 v[166:167], v[76:77], v[150:151] neg_lo:[0,1] neg_hi:[0,1]
	s_nop 0
	v_pk_fma_f32 v[166:167], v[166:167], v[166:167], v[6:7]
	v_pk_fma_f32 v[80:81], v[112:113], v[20:21], v[16:17] op_sel:[0,1,1]
	v_cmp_eq_u32_sdwa vcc, s17, v41 src0_sel:DWORD src1_sel:BYTE_2
	v_pk_fma_f32 v[80:81], v[114:115], v[36:37], v[80:81] op_sel:[0,1,0]
	ds_add_u32 v160, v162 offset:34416
	ds_add_u32 v161, v163 offset:34416
	v_cvt_pknorm_u16_f32 v158, v156, v157
	v_and_b32_e32 v159, s16, v158
	v_exp_f32_e32 v82, v80
	v_cndmask_b32_e32 v162, v164, v15, vcc
	v_cndmask_b32_e32 v152, 0, v156, vcc
	v_exp_f32_e32 v83, v81
	v_cmp_eq_u32_sdwa vcc, s17, v41 src0_sel:DWORD src1_sel:BYTE_3
	v_lshrrev_b32_sdwa v160, v165, v159 dst_sel:DWORD dst_unused:UNUSED_PAD src0_sel:DWORD src1_sel:WORD_0
	v_lshrrev_b32_sdwa v161, v165, v159 dst_sel:DWORD dst_unused:UNUSED_PAD src0_sel:DWORD src1_sel:WORD_1
	v_cndmask_b32_e32 v163, v164, v15, vcc
	v_cndmask_b32_e32 v153, 0, v157, vcc
	v_pk_fma_f32 v[154:155], v[112:113], v[8:9], v[12:13] op_sel_hi:[1,0,0]
	v_cmp_eq_u32_sdwa vcc, s18, v41 src0_sel:DWORD src1_sel:BYTE_2
	v_pk_fma_f32 v[154:155], v[114:115], v[24:25], v[154:155] op_sel_hi:[1,0,1]
	ds_add_u32 v160, v162 offset:1648
	ds_add_u32 v161, v163 offset:1648
	v_cvt_pknorm_u16_f32 v158, v82, v83
	v_and_b32_e32 v159, s16, v158
	v_exp_f32_e32 v156, v154
	v_cndmask_b32_e32 v162, v164, v15, vcc
	v_cndmask_b32_e32 v152, v152, v82, vcc
	v_exp_f32_e32 v157, v155
	v_cmp_eq_u32_sdwa vcc, s18, v41 src0_sel:DWORD src1_sel:BYTE_3
	v_lshrrev_b32_sdwa v160, v165, v159 dst_sel:DWORD dst_unused:UNUSED_PAD src0_sel:DWORD src1_sel:WORD_0
	v_lshrrev_b32_sdwa v161, v165, v159 dst_sel:DWORD dst_unused:UNUSED_PAD src0_sel:DWORD src1_sel:WORD_1
	v_cndmask_b32_e32 v163, v164, v15, vcc
	v_cndmask_b32_e32 v153, v153, v83, vcc
	v_cmp_eq_u32_sdwa vcc, s19, v41 src0_sel:DWORD src1_sel:BYTE_2
	ds_add_u32 v160, v162 offset:18032
	ds_add_u32 v161, v163 offset:18032
	v_cvt_pknorm_u16_f32 v158, v156, v157
	v_and_b32_e32 v159, s16, v158
	v_cndmask_b32_e32 v162, v164, v15, vcc
	v_cndmask_b32_e32 v152, v152, v156, vcc
	v_cmp_eq_u32_sdwa vcc, s19, v41 src0_sel:DWORD src1_sel:BYTE_3
	v_lshrrev_b32_sdwa v160, v165, v159 dst_sel:DWORD dst_unused:UNUSED_PAD src0_sel:DWORD src1_sel:WORD_0
	v_lshrrev_b32_sdwa v161, v165, v159 dst_sel:DWORD dst_unused:UNUSED_PAD src0_sel:DWORD src1_sel:WORD_1
	v_cndmask_b32_e32 v163, v164, v15, vcc
	v_cndmask_b32_e32 v153, v153, v157, vcc
	ds_add_u32 v160, v162 offset:34416
	ds_add_u32 v161, v163 offset:34416
	v_pk_add_f32 v[80:81], v[78:79], v[152:153] neg_lo:[0,1] neg_hi:[0,1]
	s_nop 0
	v_pk_fma_f32 v[6:7], v[80:81], v[80:81], v[166:167]
	ds_read_b128 v[76:79], v1 offset:61440
	v_pk_fma_f32 v[80:81], v[116:117], v[20:21], v[16:17] op_sel_hi:[1,0,0]
	v_pk_fma_f32 v[80:81], v[118:119], v[36:37], v[80:81] op_sel_hi:[1,0,1]
	s_nop 0
	v_exp_f32_e32 v82, v80
	v_exp_f32_e32 v83, v81
	v_pk_fma_f32 v[154:155], v[116:117], v[20:21], v[16:17] op_sel:[0,1,1]
	v_cmp_eq_u32_sdwa vcc, s17, v19 src0_sel:DWORD src1_sel:BYTE_0
	v_pk_fma_f32 v[154:155], v[118:119], v[36:37], v[154:155] op_sel:[0,1,0]
	v_cvt_pknorm_u16_f32 v158, v82, v83
	v_and_b32_e32 v159, s16, v158
	v_exp_f32_e32 v156, v154
	v_cndmask_b32_e32 v162, v164, v15, vcc
	v_cndmask_b32_e32 v150, 0, v82, vcc
	v_exp_f32_e32 v157, v155
	v_cmp_eq_u32_sdwa vcc, s17, v19 src0_sel:DWORD src1_sel:BYTE_1
	v_lshrrev_b32_sdwa v160, v165, v159 dst_sel:DWORD dst_unused:UNUSED_PAD src0_sel:DWORD src1_sel:WORD_0
	v_lshrrev_b32_sdwa v161, v165, v159 dst_sel:DWORD dst_unused:UNUSED_PAD src0_sel:DWORD src1_sel:WORD_1
	v_cndmask_b32_e32 v163, v164, v15, vcc
	v_cndmask_b32_e32 v151, 0, v83, vcc
	v_pk_fma_f32 v[80:81], v[116:117], v[8:9], v[12:13] op_sel_hi:[1,0,0]
	v_cmp_eq_u32_sdwa vcc, s18, v19 src0_sel:DWORD src1_sel:BYTE_0
	v_pk_fma_f32 v[80:81], v[118:119], v[24:25], v[80:81] op_sel_hi:[1,0,1]
	ds_add_u32 v160, v162 offset:1648
	ds_add_u32 v161, v163 offset:1648
	v_cvt_pknorm_u16_f32 v158, v156, v157
	v_and_b32_e32 v159, s16, v158
	v_exp_f32_e32 v82, v80
	v_cndmask_b32_e32 v162, v164, v15, vcc
	v_cndmask_b32_e32 v150, v150, v156, vcc
	v_exp_f32_e32 v83, v81
	v_cmp_eq_u32_sdwa vcc, s18, v19 src0_sel:DWORD src1_sel:BYTE_1
	v_lshrrev_b32_sdwa v160, v165, v159 dst_sel:DWORD dst_unused:UNUSED_PAD src0_sel:DWORD src1_sel:WORD_0
	v_lshrrev_b32_sdwa v161, v165, v159 dst_sel:DWORD dst_unused:UNUSED_PAD src0_sel:DWORD src1_sel:WORD_1
	v_cndmask_b32_e32 v163, v164, v15, vcc
	v_cndmask_b32_e32 v151, v151, v157, vcc
	v_pk_fma_f32 v[154:155], v[120:121], v[20:21], v[16:17] op_sel_hi:[1,0,0]
	v_cmp_eq_u32_sdwa vcc, s19, v19 src0_sel:DWORD src1_sel:BYTE_0
	v_pk_fma_f32 v[154:155], v[122:123], v[36:37], v[154:155] op_sel_hi:[1,0,1]
	ds_add_u32 v160, v162 offset:18032
	ds_add_u32 v161, v163 offset:18032
	v_cvt_pknorm_u16_f32 v158, v82, v83
	v_and_b32_e32 v159, s16, v158
	v_exp_f32_e32 v156, v154
	v_cndmask_b32_e32 v162, v164, v15, vcc
	v_cndmask_b32_e32 v150, v150, v82, vcc
	v_exp_f32_e32 v157, v155
	v_cmp_eq_u32_sdwa vcc, s19, v19 src0_sel:DWORD src1_sel:BYTE_1
	v_lshrrev_b32_sdwa v160, v165, v159 dst_sel:DWORD dst_unused:UNUSED_PAD src0_sel:DWORD src1_sel:WORD_0
	v_lshrrev_b32_sdwa v161, v165, v159 dst_sel:DWORD dst_unused:UNUSED_PAD src0_sel:DWORD src1_sel:WORD_1
	v_cndmask_b32_e32 v163, v164, v15, vcc
	v_cndmask_b32_e32 v151, v151, v83, vcc
	s_waitcnt lgkmcnt(4)
	v_pk_add_f32 v[166:167], v[76:77], v[150:151] neg_lo:[0,1] neg_hi:[0,1]
	s_nop 0
	v_pk_fma_f32 v[166:167], v[166:167], v[166:167], v[6:7]
	v_pk_fma_f32 v[80:81], v[120:121], v[20:21], v[16:17] op_sel:[0,1,1]
	v_cmp_eq_u32_sdwa vcc, s17, v19 src0_sel:DWORD src1_sel:BYTE_2
	v_pk_fma_f32 v[80:81], v[122:123], v[36:37], v[80:81] op_sel:[0,1,0]
	ds_add_u32 v160, v162 offset:34416
	ds_add_u32 v161, v163 offset:34416
	v_cvt_pknorm_u16_f32 v158, v156, v157
	v_and_b32_e32 v159, s16, v158
	v_exp_f32_e32 v82, v80
	v_cndmask_b32_e32 v162, v164, v15, vcc
	v_cndmask_b32_e32 v152, 0, v156, vcc
	v_exp_f32_e32 v83, v81
	v_cmp_eq_u32_sdwa vcc, s17, v19 src0_sel:DWORD src1_sel:BYTE_3
	v_lshrrev_b32_sdwa v160, v165, v159 dst_sel:DWORD dst_unused:UNUSED_PAD src0_sel:DWORD src1_sel:WORD_0
	v_lshrrev_b32_sdwa v161, v165, v159 dst_sel:DWORD dst_unused:UNUSED_PAD src0_sel:DWORD src1_sel:WORD_1
	v_cndmask_b32_e32 v163, v164, v15, vcc
	v_cndmask_b32_e32 v153, 0, v157, vcc
	v_pk_fma_f32 v[154:155], v[120:121], v[8:9], v[12:13] op_sel_hi:[1,0,0]
	v_cmp_eq_u32_sdwa vcc, s18, v19 src0_sel:DWORD src1_sel:BYTE_2
	v_pk_fma_f32 v[154:155], v[122:123], v[24:25], v[154:155] op_sel_hi:[1,0,1]
	ds_add_u32 v160, v162 offset:1648
	ds_add_u32 v161, v163 offset:1648
	v_cvt_pknorm_u16_f32 v158, v82, v83
	v_and_b32_e32 v159, s16, v158
	v_exp_f32_e32 v156, v154
	v_cndmask_b32_e32 v162, v164, v15, vcc
	v_cndmask_b32_e32 v152, v152, v82, vcc
	v_exp_f32_e32 v157, v155
	v_cmp_eq_u32_sdwa vcc, s18, v19 src0_sel:DWORD src1_sel:BYTE_3
	v_lshrrev_b32_sdwa v160, v165, v159 dst_sel:DWORD dst_unused:UNUSED_PAD src0_sel:DWORD src1_sel:WORD_0
	v_lshrrev_b32_sdwa v161, v165, v159 dst_sel:DWORD dst_unused:UNUSED_PAD src0_sel:DWORD src1_sel:WORD_1
	v_cndmask_b32_e32 v163, v164, v15, vcc
	v_cndmask_b32_e32 v153, v153, v83, vcc
	v_cmp_eq_u32_sdwa vcc, s19, v19 src0_sel:DWORD src1_sel:BYTE_2
	ds_add_u32 v160, v162 offset:18032
	ds_add_u32 v161, v163 offset:18032
	v_cvt_pknorm_u16_f32 v158, v156, v157
	v_and_b32_e32 v159, s16, v158
	v_cndmask_b32_e32 v162, v164, v15, vcc
	v_cndmask_b32_e32 v152, v152, v156, vcc
	v_cmp_eq_u32_sdwa vcc, s19, v19 src0_sel:DWORD src1_sel:BYTE_3
	v_lshrrev_b32_sdwa v160, v165, v159 dst_sel:DWORD dst_unused:UNUSED_PAD src0_sel:DWORD src1_sel:WORD_0
	v_lshrrev_b32_sdwa v161, v165, v159 dst_sel:DWORD dst_unused:UNUSED_PAD src0_sel:DWORD src1_sel:WORD_1
	v_cndmask_b32_e32 v163, v164, v15, vcc
	v_cndmask_b32_e32 v153, v153, v157, vcc
	ds_add_u32 v160, v162 offset:34416
	ds_add_u32 v161, v163 offset:34416
	v_pk_add_f32 v[80:81], v[78:79], v[152:153] neg_lo:[0,1] neg_hi:[0,1]
	s_nop 0
	v_pk_fma_f32 v[6:7], v[80:81], v[80:81], v[166:167]
	ds_read_b128 v[76:79], v135
	v_pk_fma_f32 v[80:81], v[58:59], v[20:21], v[16:17] op_sel_hi:[1,0,0]
	v_pk_fma_f32 v[80:81], v[124:125], v[36:37], v[80:81] op_sel_hi:[1,0,1]
	s_nop 0
	v_exp_f32_e32 v82, v80
	v_exp_f32_e32 v83, v81
	v_pk_fma_f32 v[154:155], v[58:59], v[20:21], v[16:17] op_sel:[0,1,1]
	v_cmp_eq_u32_sdwa vcc, s17, v13 src0_sel:DWORD src1_sel:BYTE_0
	v_pk_fma_f32 v[154:155], v[124:125], v[36:37], v[154:155] op_sel:[0,1,0]
	v_cvt_pknorm_u16_f32 v158, v82, v83
	v_and_b32_e32 v159, s16, v158
	v_exp_f32_e32 v156, v154
	v_cndmask_b32_e32 v162, v164, v15, vcc
	v_cndmask_b32_e32 v150, 0, v82, vcc
	v_exp_f32_e32 v157, v155
	v_cmp_eq_u32_sdwa vcc, s17, v13 src0_sel:DWORD src1_sel:BYTE_1
	v_lshrrev_b32_sdwa v160, v165, v159 dst_sel:DWORD dst_unused:UNUSED_PAD src0_sel:DWORD src1_sel:WORD_0
	v_lshrrev_b32_sdwa v161, v165, v159 dst_sel:DWORD dst_unused:UNUSED_PAD src0_sel:DWORD src1_sel:WORD_1
	v_cndmask_b32_e32 v163, v164, v15, vcc
	v_cndmask_b32_e32 v151, 0, v83, vcc
	v_pk_fma_f32 v[80:81], v[58:59], v[8:9], v[12:13] op_sel_hi:[1,0,0]
	v_cmp_eq_u32_sdwa vcc, s18, v13 src0_sel:DWORD src1_sel:BYTE_0
	v_pk_fma_f32 v[80:81], v[124:125], v[24:25], v[80:81] op_sel_hi:[1,0,1]
	ds_add_u32 v160, v162 offset:1648
	ds_add_u32 v161, v163 offset:1648
	v_cvt_pknorm_u16_f32 v158, v156, v157
	v_and_b32_e32 v159, s16, v158
	v_exp_f32_e32 v82, v80
	v_cndmask_b32_e32 v162, v164, v15, vcc
	v_cndmask_b32_e32 v150, v150, v156, vcc
	v_exp_f32_e32 v83, v81
	v_cmp_eq_u32_sdwa vcc, s18, v13 src0_sel:DWORD src1_sel:BYTE_1
	v_lshrrev_b32_sdwa v160, v165, v159 dst_sel:DWORD dst_unused:UNUSED_PAD src0_sel:DWORD src1_sel:WORD_0
	v_lshrrev_b32_sdwa v161, v165, v159 dst_sel:DWORD dst_unused:UNUSED_PAD src0_sel:DWORD src1_sel:WORD_1
	v_cndmask_b32_e32 v163, v164, v15, vcc
	v_cndmask_b32_e32 v151, v151, v157, vcc
	v_pk_fma_f32 v[154:155], v[60:61], v[20:21], v[16:17] op_sel_hi:[1,0,0]
	v_cmp_eq_u32_sdwa vcc, s19, v13 src0_sel:DWORD src1_sel:BYTE_0
	v_pk_fma_f32 v[154:155], v[126:127], v[36:37], v[154:155] op_sel_hi:[1,0,1]
	ds_add_u32 v160, v162 offset:18032
	ds_add_u32 v161, v163 offset:18032
	v_cvt_pknorm_u16_f32 v158, v82, v83
	v_and_b32_e32 v159, s16, v158
	v_exp_f32_e32 v156, v154
	v_cndmask_b32_e32 v162, v164, v15, vcc
	v_cndmask_b32_e32 v150, v150, v82, vcc
	v_exp_f32_e32 v157, v155
	v_cmp_eq_u32_sdwa vcc, s19, v13 src0_sel:DWORD src1_sel:BYTE_1
	v_lshrrev_b32_sdwa v160, v165, v159 dst_sel:DWORD dst_unused:UNUSED_PAD src0_sel:DWORD src1_sel:WORD_0
	v_lshrrev_b32_sdwa v161, v165, v159 dst_sel:DWORD dst_unused:UNUSED_PAD src0_sel:DWORD src1_sel:WORD_1
	v_cndmask_b32_e32 v163, v164, v15, vcc
	v_cndmask_b32_e32 v151, v151, v83, vcc
	s_waitcnt lgkmcnt(4)
	v_pk_add_f32 v[166:167], v[76:77], v[150:151] neg_lo:[0,1] neg_hi:[0,1]
	s_nop 0
	v_pk_fma_f32 v[166:167], v[166:167], v[166:167], v[6:7]
	v_pk_fma_f32 v[80:81], v[60:61], v[20:21], v[16:17] op_sel:[0,1,1]
	v_cmp_eq_u32_sdwa vcc, s17, v13 src0_sel:DWORD src1_sel:BYTE_2
	v_pk_fma_f32 v[80:81], v[126:127], v[36:37], v[80:81] op_sel:[0,1,0]
	ds_add_u32 v160, v162 offset:34416
	ds_add_u32 v161, v163 offset:34416
	v_cvt_pknorm_u16_f32 v158, v156, v157
	v_and_b32_e32 v159, s16, v158
	v_exp_f32_e32 v82, v80
	v_cndmask_b32_e32 v162, v164, v15, vcc
	v_cndmask_b32_e32 v152, 0, v156, vcc
	v_exp_f32_e32 v83, v81
	v_cmp_eq_u32_sdwa vcc, s17, v13 src0_sel:DWORD src1_sel:BYTE_3
	v_lshrrev_b32_sdwa v160, v165, v159 dst_sel:DWORD dst_unused:UNUSED_PAD src0_sel:DWORD src1_sel:WORD_0
	v_lshrrev_b32_sdwa v161, v165, v159 dst_sel:DWORD dst_unused:UNUSED_PAD src0_sel:DWORD src1_sel:WORD_1
	v_cndmask_b32_e32 v163, v164, v15, vcc
	v_cndmask_b32_e32 v153, 0, v157, vcc
	v_pk_fma_f32 v[154:155], v[60:61], v[8:9], v[12:13] op_sel_hi:[1,0,0]
	v_cmp_eq_u32_sdwa vcc, s18, v13 src0_sel:DWORD src1_sel:BYTE_2
	v_pk_fma_f32 v[154:155], v[126:127], v[24:25], v[154:155] op_sel_hi:[1,0,1]
	ds_add_u32 v160, v162 offset:1648
	ds_add_u32 v161, v163 offset:1648
	v_cvt_pknorm_u16_f32 v158, v82, v83
	v_and_b32_e32 v159, s16, v158
	v_exp_f32_e32 v156, v154
	v_cndmask_b32_e32 v162, v164, v15, vcc
	v_cndmask_b32_e32 v152, v152, v82, vcc
	v_exp_f32_e32 v157, v155
	v_cmp_eq_u32_sdwa vcc, s18, v13 src0_sel:DWORD src1_sel:BYTE_3
	v_lshrrev_b32_sdwa v160, v165, v159 dst_sel:DWORD dst_unused:UNUSED_PAD src0_sel:DWORD src1_sel:WORD_0
	v_lshrrev_b32_sdwa v161, v165, v159 dst_sel:DWORD dst_unused:UNUSED_PAD src0_sel:DWORD src1_sel:WORD_1
	v_cndmask_b32_e32 v163, v164, v15, vcc
	v_cndmask_b32_e32 v153, v153, v83, vcc
	v_cmp_eq_u32_sdwa vcc, s19, v13 src0_sel:DWORD src1_sel:BYTE_2
	ds_add_u32 v160, v162 offset:18032
	ds_add_u32 v161, v163 offset:18032
	v_cvt_pknorm_u16_f32 v158, v156, v157
	v_and_b32_e32 v159, s16, v158
	v_cndmask_b32_e32 v162, v164, v15, vcc
	v_cndmask_b32_e32 v152, v152, v156, vcc
	v_cmp_eq_u32_sdwa vcc, s19, v13 src0_sel:DWORD src1_sel:BYTE_3
	v_lshrrev_b32_sdwa v160, v165, v159 dst_sel:DWORD dst_unused:UNUSED_PAD src0_sel:DWORD src1_sel:WORD_0
	v_lshrrev_b32_sdwa v161, v165, v159 dst_sel:DWORD dst_unused:UNUSED_PAD src0_sel:DWORD src1_sel:WORD_1
	v_cndmask_b32_e32 v163, v164, v15, vcc
	v_cndmask_b32_e32 v153, v153, v157, vcc
	ds_add_u32 v160, v162 offset:34416
	ds_add_u32 v161, v163 offset:34416
	v_pk_add_f32 v[80:81], v[78:79], v[152:153] neg_lo:[0,1] neg_hi:[0,1]
	s_nop 0
	v_pk_fma_f32 v[6:7], v[80:81], v[80:81], v[166:167]
	ds_read_b128 v[76:79], v70
	v_pk_fma_f32 v[80:81], v[62:63], v[20:21], v[16:17] op_sel_hi:[1,0,0]
	v_pk_fma_f32 v[80:81], v[66:67], v[36:37], v[80:81] op_sel_hi:[1,0,1]
	s_nop 0
	v_exp_f32_e32 v82, v80
	v_exp_f32_e32 v83, v81
	v_pk_fma_f32 v[154:155], v[62:63], v[20:21], v[16:17] op_sel:[0,1,1]
	v_cmp_eq_u32_sdwa vcc, s17, v9 src0_sel:DWORD src1_sel:BYTE_0
	v_pk_fma_f32 v[154:155], v[66:67], v[36:37], v[154:155] op_sel:[0,1,0]
	v_cvt_pknorm_u16_f32 v158, v82, v83
	v_and_b32_e32 v159, s16, v158
	v_exp_f32_e32 v156, v154
	v_cndmask_b32_e32 v162, v164, v15, vcc
	v_cndmask_b32_e32 v150, 0, v82, vcc
	v_exp_f32_e32 v157, v155
	v_cmp_eq_u32_sdwa vcc, s17, v9 src0_sel:DWORD src1_sel:BYTE_1
	v_lshrrev_b32_sdwa v160, v165, v159 dst_sel:DWORD dst_unused:UNUSED_PAD src0_sel:DWORD src1_sel:WORD_0
	v_lshrrev_b32_sdwa v161, v165, v159 dst_sel:DWORD dst_unused:UNUSED_PAD src0_sel:DWORD src1_sel:WORD_1
	v_cndmask_b32_e32 v163, v164, v15, vcc
	v_cndmask_b32_e32 v151, 0, v83, vcc
	v_pk_fma_f32 v[80:81], v[62:63], v[8:9], v[12:13] op_sel_hi:[1,0,0]
	v_cmp_eq_u32_sdwa vcc, s18, v9 src0_sel:DWORD src1_sel:BYTE_0
	v_pk_fma_f32 v[80:81], v[66:67], v[24:25], v[80:81] op_sel_hi:[1,0,1]
	ds_add_u32 v160, v162 offset:1648
	ds_add_u32 v161, v163 offset:1648
	v_cvt_pknorm_u16_f32 v158, v156, v157
	v_and_b32_e32 v159, s16, v158
	v_exp_f32_e32 v82, v80
	v_cndmask_b32_e32 v162, v164, v15, vcc
	v_cndmask_b32_e32 v150, v150, v156, vcc
	v_exp_f32_e32 v83, v81
	v_cmp_eq_u32_sdwa vcc, s18, v9 src0_sel:DWORD src1_sel:BYTE_1
	v_lshrrev_b32_sdwa v160, v165, v159 dst_sel:DWORD dst_unused:UNUSED_PAD src0_sel:DWORD src1_sel:WORD_0
	v_lshrrev_b32_sdwa v161, v165, v159 dst_sel:DWORD dst_unused:UNUSED_PAD src0_sel:DWORD src1_sel:WORD_1
	v_cndmask_b32_e32 v163, v164, v15, vcc
	v_cndmask_b32_e32 v151, v151, v157, vcc
	v_pk_fma_f32 v[154:155], v[64:65], v[20:21], v[16:17] op_sel_hi:[1,0,0]
	v_cmp_eq_u32_sdwa vcc, s19, v9 src0_sel:DWORD src1_sel:BYTE_0
	v_pk_fma_f32 v[154:155], v[68:69], v[36:37], v[154:155] op_sel_hi:[1,0,1]
	ds_add_u32 v160, v162 offset:18032
	ds_add_u32 v161, v163 offset:18032
	v_cvt_pknorm_u16_f32 v158, v82, v83
	v_and_b32_e32 v159, s16, v158
	v_exp_f32_e32 v156, v154
	v_cndmask_b32_e32 v162, v164, v15, vcc
	v_cndmask_b32_e32 v150, v150, v82, vcc
	v_exp_f32_e32 v157, v155
	v_cmp_eq_u32_sdwa vcc, s19, v9 src0_sel:DWORD src1_sel:BYTE_1
	v_lshrrev_b32_sdwa v160, v165, v159 dst_sel:DWORD dst_unused:UNUSED_PAD src0_sel:DWORD src1_sel:WORD_0
	v_lshrrev_b32_sdwa v161, v165, v159 dst_sel:DWORD dst_unused:UNUSED_PAD src0_sel:DWORD src1_sel:WORD_1
	v_cndmask_b32_e32 v163, v164, v15, vcc
	v_cndmask_b32_e32 v151, v151, v83, vcc
	s_waitcnt lgkmcnt(4)
	v_pk_add_f32 v[166:167], v[76:77], v[150:151] neg_lo:[0,1] neg_hi:[0,1]
	s_nop 0
	v_pk_fma_f32 v[166:167], v[166:167], v[166:167], v[6:7]
	v_pk_fma_f32 v[80:81], v[64:65], v[20:21], v[16:17] op_sel:[0,1,1]
	v_cmp_eq_u32_sdwa vcc, s17, v9 src0_sel:DWORD src1_sel:BYTE_2
	v_pk_fma_f32 v[80:81], v[68:69], v[36:37], v[80:81] op_sel:[0,1,0]
	ds_add_u32 v160, v162 offset:34416
	ds_add_u32 v161, v163 offset:34416
	v_cvt_pknorm_u16_f32 v158, v156, v157
	v_and_b32_e32 v159, s16, v158
	v_exp_f32_e32 v82, v80
	v_cndmask_b32_e32 v162, v164, v15, vcc
	v_cndmask_b32_e32 v152, 0, v156, vcc
	v_exp_f32_e32 v83, v81
	v_cmp_eq_u32_sdwa vcc, s17, v9 src0_sel:DWORD src1_sel:BYTE_3
	v_lshrrev_b32_sdwa v160, v165, v159 dst_sel:DWORD dst_unused:UNUSED_PAD src0_sel:DWORD src1_sel:WORD_0
	v_lshrrev_b32_sdwa v161, v165, v159 dst_sel:DWORD dst_unused:UNUSED_PAD src0_sel:DWORD src1_sel:WORD_1
	v_cndmask_b32_e32 v163, v164, v15, vcc
	v_cndmask_b32_e32 v153, 0, v157, vcc
	v_pk_fma_f32 v[154:155], v[64:65], v[8:9], v[12:13] op_sel_hi:[1,0,0]
	v_cmp_eq_u32_sdwa vcc, s18, v9 src0_sel:DWORD src1_sel:BYTE_2
	v_pk_fma_f32 v[154:155], v[68:69], v[24:25], v[154:155] op_sel_hi:[1,0,1]
	ds_add_u32 v160, v162 offset:1648
	ds_add_u32 v161, v163 offset:1648
	v_cvt_pknorm_u16_f32 v158, v82, v83
	v_and_b32_e32 v159, s16, v158
	v_exp_f32_e32 v156, v154
	v_cndmask_b32_e32 v162, v164, v15, vcc
	v_cndmask_b32_e32 v152, v152, v82, vcc
	v_exp_f32_e32 v157, v155
	v_cmp_eq_u32_sdwa vcc, s18, v9 src0_sel:DWORD src1_sel:BYTE_3
	v_lshrrev_b32_sdwa v160, v165, v159 dst_sel:DWORD dst_unused:UNUSED_PAD src0_sel:DWORD src1_sel:WORD_0
	v_lshrrev_b32_sdwa v161, v165, v159 dst_sel:DWORD dst_unused:UNUSED_PAD src0_sel:DWORD src1_sel:WORD_1
	v_cndmask_b32_e32 v163, v164, v15, vcc
	v_cndmask_b32_e32 v153, v153, v83, vcc
	v_cmp_eq_u32_sdwa vcc, s19, v9 src0_sel:DWORD src1_sel:BYTE_2
	ds_add_u32 v160, v162 offset:18032
	ds_add_u32 v161, v163 offset:18032
	v_cvt_pknorm_u16_f32 v158, v156, v157
	v_and_b32_e32 v159, s16, v158
	v_cndmask_b32_e32 v162, v164, v15, vcc
	v_cndmask_b32_e32 v152, v152, v156, vcc
	v_cmp_eq_u32_sdwa vcc, s19, v9 src0_sel:DWORD src1_sel:BYTE_3
	v_lshrrev_b32_sdwa v160, v165, v159 dst_sel:DWORD dst_unused:UNUSED_PAD src0_sel:DWORD src1_sel:WORD_0
	v_lshrrev_b32_sdwa v161, v165, v159 dst_sel:DWORD dst_unused:UNUSED_PAD src0_sel:DWORD src1_sel:WORD_1
	v_cndmask_b32_e32 v163, v164, v15, vcc
	v_cndmask_b32_e32 v153, v153, v157, vcc
	ds_add_u32 v160, v162 offset:34416
	ds_add_u32 v161, v163 offset:34416
	v_pk_add_f32 v[80:81], v[78:79], v[152:153] neg_lo:[0,1] neg_hi:[0,1]
	s_nop 0
	v_pk_fma_f32 v[6:7], v[80:81], v[80:81], v[166:167]
	s_and_saveexec_b64 s[8:9], s[4:5]
	s_cbranch_execz .LBB0_60
	v_add_u32_e32 v149, 0x18000, v1
	ds_read_b128 v[76:79], v149
	v_pk_fma_f32 v[80:81], v[54:55], v[20:21], v[16:17] op_sel_hi:[1,0,0]
	v_pk_fma_f32 v[80:81], v[50:51], v[36:37], v[80:81] op_sel_hi:[1,0,1]
	s_nop 0
	v_exp_f32_e32 v82, v80
	v_exp_f32_e32 v83, v81
	v_pk_fma_f32 v[154:155], v[54:55], v[20:21], v[16:17] op_sel:[0,1,1]
	v_cmp_eq_u32_sdwa vcc, s17, v40 src0_sel:DWORD src1_sel:BYTE_0
	v_pk_fma_f32 v[154:155], v[50:51], v[36:37], v[154:155] op_sel:[0,1,0]
	v_cvt_pknorm_u16_f32 v158, v82, v83
	v_and_b32_e32 v159, s16, v158
	v_exp_f32_e32 v156, v154
	v_cndmask_b32_e32 v162, v164, v15, vcc
	v_cndmask_b32_e32 v150, 0, v82, vcc
	v_exp_f32_e32 v157, v155
	v_cmp_eq_u32_sdwa vcc, s17, v40 src0_sel:DWORD src1_sel:BYTE_1
	v_lshrrev_b32_sdwa v160, v165, v159 dst_sel:DWORD dst_unused:UNUSED_PAD src0_sel:DWORD src1_sel:WORD_0
	v_lshrrev_b32_sdwa v161, v165, v159 dst_sel:DWORD dst_unused:UNUSED_PAD src0_sel:DWORD src1_sel:WORD_1
	v_cndmask_b32_e32 v163, v164, v15, vcc
	v_cndmask_b32_e32 v151, 0, v83, vcc
	v_pk_fma_f32 v[80:81], v[54:55], v[8:9], v[12:13] op_sel_hi:[1,0,0]
	v_cmp_eq_u32_sdwa vcc, s18, v40 src0_sel:DWORD src1_sel:BYTE_0
	v_pk_fma_f32 v[80:81], v[50:51], v[24:25], v[80:81] op_sel_hi:[1,0,1]
	ds_add_u32 v160, v162 offset:1648
	ds_add_u32 v161, v163 offset:1648
	v_cvt_pknorm_u16_f32 v158, v156, v157
	v_and_b32_e32 v159, s16, v158
	v_exp_f32_e32 v82, v80
	v_cndmask_b32_e32 v162, v164, v15, vcc
	v_cndmask_b32_e32 v150, v150, v156, vcc
	v_exp_f32_e32 v83, v81
	v_cmp_eq_u32_sdwa vcc, s18, v40 src0_sel:DWORD src1_sel:BYTE_1
	v_lshrrev_b32_sdwa v160, v165, v159 dst_sel:DWORD dst_unused:UNUSED_PAD src0_sel:DWORD src1_sel:WORD_0
	v_lshrrev_b32_sdwa v161, v165, v159 dst_sel:DWORD dst_unused:UNUSED_PAD src0_sel:DWORD src1_sel:WORD_1
	v_cndmask_b32_e32 v163, v164, v15, vcc
	v_cndmask_b32_e32 v151, v151, v157, vcc
	v_pk_fma_f32 v[154:155], v[46:47], v[20:21], v[16:17] op_sel_hi:[1,0,0]
	v_cmp_eq_u32_sdwa vcc, s19, v40 src0_sel:DWORD src1_sel:BYTE_0
	v_pk_fma_f32 v[154:155], v[74:75], v[36:37], v[154:155] op_sel_hi:[1,0,1]
	ds_add_u32 v160, v162 offset:18032
	ds_add_u32 v161, v163 offset:18032
	v_cvt_pknorm_u16_f32 v158, v82, v83
	v_and_b32_e32 v159, s16, v158
	v_exp_f32_e32 v156, v154
	v_cndmask_b32_e32 v162, v164, v15, vcc
	v_cndmask_b32_e32 v150, v150, v82, vcc
	v_exp_f32_e32 v157, v155
	v_cmp_eq_u32_sdwa vcc, s19, v40 src0_sel:DWORD src1_sel:BYTE_1
	v_lshrrev_b32_sdwa v160, v165, v159 dst_sel:DWORD dst_unused:UNUSED_PAD src0_sel:DWORD src1_sel:WORD_0
	v_lshrrev_b32_sdwa v161, v165, v159 dst_sel:DWORD dst_unused:UNUSED_PAD src0_sel:DWORD src1_sel:WORD_1
	v_cndmask_b32_e32 v163, v164, v15, vcc
	v_cndmask_b32_e32 v151, v151, v83, vcc
	s_waitcnt lgkmcnt(4)
	v_pk_add_f32 v[166:167], v[76:77], v[150:151] neg_lo:[0,1] neg_hi:[0,1]
	s_nop 0
	v_pk_fma_f32 v[166:167], v[166:167], v[166:167], v[6:7]
	v_pk_fma_f32 v[80:81], v[46:47], v[20:21], v[16:17] op_sel:[0,1,1]
	v_cmp_eq_u32_sdwa vcc, s17, v40 src0_sel:DWORD src1_sel:BYTE_2
	v_pk_fma_f32 v[80:81], v[74:75], v[36:37], v[80:81] op_sel:[0,1,0]
	ds_add_u32 v160, v162 offset:34416
	ds_add_u32 v161, v163 offset:34416
	v_cvt_pknorm_u16_f32 v158, v156, v157
	v_and_b32_e32 v159, s16, v158
	v_exp_f32_e32 v82, v80
	v_cndmask_b32_e32 v162, v164, v15, vcc
	v_cndmask_b32_e32 v152, 0, v156, vcc
	v_exp_f32_e32 v83, v81
	v_cmp_eq_u32_sdwa vcc, s17, v40 src0_sel:DWORD src1_sel:BYTE_3
	v_lshrrev_b32_sdwa v160, v165, v159 dst_sel:DWORD dst_unused:UNUSED_PAD src0_sel:DWORD src1_sel:WORD_0
	v_lshrrev_b32_sdwa v161, v165, v159 dst_sel:DWORD dst_unused:UNUSED_PAD src0_sel:DWORD src1_sel:WORD_1
	v_cndmask_b32_e32 v163, v164, v15, vcc
	v_cndmask_b32_e32 v153, 0, v157, vcc
	v_pk_fma_f32 v[154:155], v[46:47], v[8:9], v[12:13] op_sel_hi:[1,0,0]
	v_cmp_eq_u32_sdwa vcc, s18, v40 src0_sel:DWORD src1_sel:BYTE_2
	v_pk_fma_f32 v[154:155], v[74:75], v[24:25], v[154:155] op_sel_hi:[1,0,1]
	ds_add_u32 v160, v162 offset:1648
	ds_add_u32 v161, v163 offset:1648
	v_cvt_pknorm_u16_f32 v158, v82, v83
	v_and_b32_e32 v159, s16, v158
	v_exp_f32_e32 v156, v154
	v_cndmask_b32_e32 v162, v164, v15, vcc
	v_cndmask_b32_e32 v152, v152, v82, vcc
	v_exp_f32_e32 v157, v155
	v_cmp_eq_u32_sdwa vcc, s18, v40 src0_sel:DWORD src1_sel:BYTE_3
	v_lshrrev_b32_sdwa v160, v165, v159 dst_sel:DWORD dst_unused:UNUSED_PAD src0_sel:DWORD src1_sel:WORD_0
	v_lshrrev_b32_sdwa v161, v165, v159 dst_sel:DWORD dst_unused:UNUSED_PAD src0_sel:DWORD src1_sel:WORD_1
	v_cndmask_b32_e32 v163, v164, v15, vcc
	v_cndmask_b32_e32 v153, v153, v83, vcc
	v_cmp_eq_u32_sdwa vcc, s19, v40 src0_sel:DWORD src1_sel:BYTE_2
	ds_add_u32 v160, v162 offset:18032
	ds_add_u32 v161, v163 offset:18032
	v_cvt_pknorm_u16_f32 v158, v156, v157
	v_and_b32_e32 v159, s16, v158
	v_cndmask_b32_e32 v162, v164, v15, vcc
	v_cndmask_b32_e32 v152, v152, v156, vcc
	v_cmp_eq_u32_sdwa vcc, s19, v40 src0_sel:DWORD src1_sel:BYTE_3
	v_lshrrev_b32_sdwa v160, v165, v159 dst_sel:DWORD dst_unused:UNUSED_PAD src0_sel:DWORD src1_sel:WORD_0
	v_lshrrev_b32_sdwa v161, v165, v159 dst_sel:DWORD dst_unused:UNUSED_PAD src0_sel:DWORD src1_sel:WORD_1
	v_cndmask_b32_e32 v163, v164, v15, vcc
	v_cndmask_b32_e32 v153, v153, v157, vcc
	ds_add_u32 v160, v162 offset:34416
	ds_add_u32 v161, v163 offset:34416
	v_pk_add_f32 v[80:81], v[78:79], v[152:153] neg_lo:[0,1] neg_hi:[0,1]
	s_nop 0
	v_pk_fma_f32 v[6:7], v[80:81], v[80:81], v[166:167]
